# placement: expert GEMM loops at offset 32 mod 64
# speedup vs baseline: 1.0001x; 1.0001x over previous
;     __device__ __forceinline__ bool next(int i, Unit& u) const { if (!order_tile(i, G, c, nM, nN, u.pm, u.pn)) return false; u.A = A0 + (size_t)u.pm * tstep; u.B = B0 + (size_t)u.pn * tstep; return true; }
;     __device__ __forceinline__ bool next(int i, Unit& u) const { if (!order_tile(i, G, c, nM, nN, u.pm, u.pn)) return false; u.A = A0 + (size_t)(u.pn >> 1) * groupA + (size_t)u.pm * tstep; u.B = B0 + (size_t)u.pn * tstep; return true; }
; __device__ __forceinline__ bool order_tile(int i, int G, int c, int nM, int nN, int& pm, int& pn) {
;     const int nwg = nM * nN; const int L = i * G + c; if (L >= nwg) return false;
;     int wgid = L; { const int q = nwg / NXCD, r = nwg % NXCD, xcd = wgid % NXCD, off = wgid / NXCD; wgid = (xcd < r ? xcd * (q + 1) : r * (q + 1) + (xcd - r) * q) + off; }
;     const int nig = WGM * nN, gid = wgid / nig, fm = gid * WGM, gsz = (nM - fm) < WGM ? (nM - fm) : WGM;
;     pm = fm + ((wgid % nig) % gsz); pn = (wgid % nig) / gsz; return true;
; }
;     __device__ __forceinline__ bool next(int i, Unit& u) const { if (!order_tile(i, G, c, nM, nN, u.pm, u.pn)) return false; const int e = cum.expert(u.pm + pm0);
;         u.A = A0 + (size_t)u.pm * tstep; u.B = B0 + (size_t)e * expB + (size_t)u.pn * tstep; return true; }
.LBB0_2748:
	v_readlane_b32 s2, v241, 5
	v_readlane_b32 s3, v241, 6
	s_add_u32 s2, s2, 0x31500000
	s_addc_u32 s3, s3, 0
	s_lshl_b32 s6, s6, 5
	s_and_b32 s55, s6, 0x60
	s_lshl_b32 s54, s7, 6
	s_lshl_b32 s8, s7, 13
	s_lshl_b32 s9, s55, 7
	s_add_u32 s6, s24, 0x80
	s_addc_u32 s7, s25, 0
	s_add_i32 s57, s19, 0x18000
	s_waitcnt vmcnt(4)
	s_barrier
	s_mov_b32 s10, m0
	s_mov_b32 m0, s57
	s_nop 0
	global_load_lds_dwordx4 v138, s[6:7]
	s_mov_b32 m0, s10
	s_add_u32 s6, s24, 0x20080
	s_addc_u32 s7, s25, 0
	s_add_i32 s58, s19, 0x1a000
	s_mov_b32 s10, m0
	s_mov_b32 m0, s58
	s_nop 0
	global_load_lds_dwordx4 v138, s[6:7]
	s_mov_b32 m0, s10
	s_add_u32 s6, s22, 0x80
	s_addc_u32 s7, s23, 0
	s_add_i32 s59, s19, 0x8000
	s_mov_b32 s10, m0
	s_mov_b32 m0, s59
	s_nop 0
	global_load_lds_dwordx4 v1, s[6:7]
	s_mov_b32 m0, s10
	s_add_u32 s6, s22, 0x20080
	s_addc_u32 s7, s23, 0
	s_add_i32 s60, s19, 0xa000
	s_mov_b32 s10, m0
	s_mov_b32 m0, s60
	s_nop 0
	global_load_lds_dwordx4 v1, s[6:7]
	s_mov_b32 m0, s10
	s_add_u32 s6, s24, 0x40080
	s_addc_u32 s7, s25, 0
	s_add_i32 s61, s19, 0x1c000
	v_lshlrev_b32_e32 v3, 6, v0
	v_lshlrev_b32_e32 v4, 2, v0
	s_mov_b32 s10, m0
	s_mov_b32 m0, s61
	s_nop 0
	global_load_lds_dwordx4 v138, s[6:7]
	s_mov_b32 m0, s10
	s_add_u32 s6, s24, 0x60080
	v_and_b32_e32 v2, 48, v0
	v_and_b32_e32 v3, 0x3c0, v3
	v_and_b32_e32 v4, 32, v4
	s_addc_u32 s7, s25, 0
	s_add_i32 s62, s19, 0x1e000
	s_mov_b32 s10, m0
	s_mov_b32 m0, s62
	s_nop 0
	global_load_lds_dwordx4 v138, s[6:7]
	s_mov_b32 m0, s10
	v_bitop3_b32 v2, v3, v4, v2 bitop3:0x36
	s_waitcnt vmcnt(6)
	s_add_i32 s6, s9, 0
	v_add_u32_e32 v3, s6, v2
	v_add_u32_e32 v2, 0, v2
	s_mov_b32 s6, 0x39000000
	s_mov_b32 s56, 0
	s_add_i32 s63, s19, 0xc000
	v_add_u32_e32 v139, 0x10000, v3
	v_add_u32_e32 v140, 0x10400, v3
	v_add_u32_e32 v141, 0x10800, v3
	v_add_u32_e32 v142, 0x10c00, v3
	s_add_i32 s64, s19, 0xe000
	v_add_u32_e32 v143, 0x14000, v3
	v_add_u32_e32 v144, 0x14400, v3
	v_add_u32_e32 v145, 0x14800, v3
	v_add_u32_e32 v146, 0x14c00, v3
	v_add_u32_e32 v147, 0x18000, v3
	v_add_u32_e32 v148, 0x18400, v3
	v_add_u32_e32 v149, 0x18800, v3
	v_add_u32_e32 v150, 0x18c00, v3
	v_add_u32_e32 v151, 0x1c000, v3
	v_add_u32_e32 v152, 0x1c400, v3
	v_add_u32_e32 v153, 0x1c800, v3
	v_add_u32_e32 v154, 0x1cc00, v3
	v_add_u32_e32 v155, s8, v2
	v_mov_b32_e32 v156, 0x7f7f7f7f
	s_movk_i32 s65, 0x1c00
	s_mov_b32 s7, 0x3a800000
	s_mov_b32 s66, 0xc3e00000
	v_mov_b32_e32 v157, 0x43e00000
	s_mov_b64 s[16:17], s[24:25]
	s_mov_b64 s[14:15], s[22:23]
	s_barrier
	s_nop 0
	s_nop 0
	s_nop 0
	s_nop 0
	s_nop 0
	s_nop 0
	s_nop 0
	s_nop 0
	s_nop 0
	s_nop 0
	s_nop 0
	s_nop 0
.LBB0_2749:
	s_add_i32 s56, s56, 1
	v_readlane_b32 s8, v241, 42
	s_mul_i32 s11, s56, s8
	s_add_i32 s11, s11, s79
	s_cmp_ge_i32 s11, s43
	s_cselect_b64 s[8:9], -1, 0
	s_and_b64 vcc, exec, s[8:9]
	s_cbranch_vccnz .LBB0_2751
	s_ashr_i32 s10, s11, 31
	s_lshr_b32 s10, s10, 29
	s_add_i32 s10, s11, s10
	s_ashr_i32 s12, s10, 3
	s_and_b32 s10, s10, -8
	s_sub_i32 s10, s11, s10
	s_cmp_lt_i32 s10, 0
	s_cselect_b32 s11, s47, s46
	s_mul_i32 s10, s10, s11
	s_add_i32 s10, s10, s12
	s_mul_hi_i32 s11, s10, 0x92492493
	s_add_i32 s11, s11, s10
	s_lshr_b32 s12, s11, 31
	s_ashr_i32 s11, s11, 8
	s_add_i32 s11, s11, s12
	s_lshl_b32 s12, s11, 3
	s_sub_i32 s13, s35, s12
	s_min_i32 s13, s13, 8
	s_abs_i32 s14, s13
	v_cvt_f32_u32_e32 v2, s14
	s_sub_i32 s16, 0, s14
	s_mulk_i32 s11, 0x1c0
	s_sub_i32 s11, s10, s11
	v_rcp_iflag_f32_e32 v2, v2
	s_abs_i32 s10, s11
	s_xor_b32 s15, s11, s13
	s_ashr_i32 s15, s15, 31
	v_mul_f32_e32 v2, 0x4f7ffffe, v2
	v_cvt_u32_f32_e32 v2, v2
	s_nop 0
	v_readfirstlane_b32 s17, v2
	s_mul_i32 s16, s16, s17
	s_mul_hi_u32 s16, s17, s16
	s_add_i32 s17, s17, s16
	s_mul_hi_u32 s16, s10, s17
	s_mul_i32 s17, s16, s14
	s_sub_i32 s10, s10, s17
	s_add_i32 s26, s16, 1
	s_sub_i32 s17, s10, s14
	s_cmp_ge_u32 s10, s14
	s_cselect_b32 s16, s26, s16
	s_cselect_b32 s10, s17, s10
	s_add_i32 s17, s16, 1
	s_cmp_ge_u32 s10, s14
	s_cselect_b32 s10, s17, s16
	s_xor_b32 s10, s10, s15
	s_sub_i32 s10, s10, s15
	s_mul_i32 s13, s10, s13
	s_sub_i32 s11, s11, s13
	s_add_i32 s12, s12, s11
	s_cmp_ge_i32 s12, s0
	s_cselect_b64 s[14:15], -1, 0
	s_cmp_ge_i32 s12, s36
	s_cselect_b64 s[16:17], -1, 0
	s_cmp_ge_i32 s12, s37
	v_cndmask_b32_e64 v2, 0, 1, s[16:17]
	v_cndmask_b32_e64 v3, 0, 1, s[14:15]
	s_cselect_b64 s[14:15], -1, 0
	v_readfirstlane_b32 s11, v2
	v_readfirstlane_b32 s13, v3
	s_cmp_lg_u64 s[14:15], 0
	s_addc_u32 s11, s11, s13
	s_cmp_ge_i32 s12, s38
	s_cselect_b64 s[14:15], -1, 0
	v_cndmask_b32_e64 v2, 0, 1, s[14:15]
	s_nop 0
	v_readfirstlane_b32 s13, v2
	s_add_u32 s11, s11, s13
	s_addc_u32 s13, 0, 0
	s_cmp_ge_i32 s12, s39
	s_cselect_b64 s[14:15], -1, 0
	v_cndmask_b32_e64 v2, 0, 1, s[14:15]
	s_nop 0
	v_readfirstlane_b32 s14, v2
	s_add_u32 s11, s11, s14
	s_addc_u32 s13, s13, 0
	s_cmp_ge_i32 s12, s40
	s_cselect_b64 s[14:15], -1, 0
	v_cndmask_b32_e64 v2, 0, 1, s[14:15]
	s_nop 0
	v_readfirstlane_b32 s14, v2
	s_add_u32 s11, s11, s14
	s_addc_u32 s13, s13, 0
	s_cmp_ge_i32 s12, s41
	s_cselect_b64 s[14:15], -1, 0
	v_cndmask_b32_e64 v2, 0, 1, s[14:15]
	s_nop 0
	v_readfirstlane_b32 s14, v2
	s_add_u32 s11, s11, s14
	s_addc_u32 s16, s13, 0
	s_ashr_i32 s13, s12, 31
	s_lshl_b64 s[14:15], s[12:13], 19
	s_add_u32 s14, s44, s14
	s_mul_i32 s16, s16, 0x1c00000
	s_mul_hi_u32 s13, s11, 0x1c00000
	s_addc_u32 s15, s45, s15
	s_add_i32 s13, s13, s16
	s_mul_i32 s11, s11, 0x1c00000
	s_add_u32 s26, s33, s11
	s_addc_u32 s13, s34, s13
	s_ashr_i32 s11, s10, 31
	s_lshl_b64 s[16:17], s[10:11], 19
	s_add_u32 s16, s26, s16
	s_addc_u32 s17, s13, s17
